# split-phase SEAM(9) plus conversion share of the non-attention workgroups raised from 24 to 27 of 28 items per wave pair
# speedup vs baseline: 1.0045x; 1.0008x over previous
; #define LAS __attribute__((address_space(3)))
; __device__ __forceinline__ void convert_items(Frame& F, const Args& a, int lo, int hi, int w, int nw) {
;     const int lane = pg8::pg8_lane_id();
;     LAS float* scr = (LAS float*)(F.lds + RING_OFF + F.wave * 8448);
;     constexpr int I_FI = CONV_I_FI, I_FO = CONV_I_FO, I_SI = CONV_I_SI, I_SO = CONV_I_SO, I_GU = CONV_I_GU, I_DN = CONV_I_DN;
;     for (int it = lo + w; it < hi; it += nw) {
;         int r = it;
;         if (r < I_FI) { tr_item(a.in[7], 3 * D + 16, D, 96, r, (bf16*)(F.ws + WS_WFOXIN), false, scr, lane); continue; } r -= I_FI;
;         if (r < I_FO) { tr_item(a.in[9], D, D, 32, r, (bf16*)(F.ws + WS_WFOXOUT), false, scr, lane); continue; } r -= I_FO;
;         if (r < I_SI) { tr_item(a.in[10], D + 512, D, 48, r, (bf16*)(F.ws + WS_WSWAIN), false, scr, lane); continue; } r -= I_SI;
;         if (r < I_SO) { tr_item(a.in[12], D, D, 32, r, (bf16*)(F.ws + WS_WSWAOUT), false, scr, lane); continue; } r -= I_SO;
;         if (r < I_GU) { tr_item8(a.in[14], 2 * FF, D, 224, r, F.ws + WS_WGU, true, WSC_GU, scr, lane); continue; } r -= I_GU;
;         if (r < I_DN) { tr_item8(a.in[15], D, FF, 32, r, F.ws + WS_WDN, false, WSC_DN, scr, lane); continue; } r -= I_DN;
;         if (r < NE * I_GU) { const int e = r / I_GU, rr = r % I_GU; tr_item8(a.in[18] + (size_t)e * D * 2 * FF, 2 * FF, D, 224, rr, F.ws + WS_WMGU + (size_t)e * 2 * FF * D, true, WSC_GU, scr, lane); continue; } r -= NE * I_GU;
; __global__ void __launch_bounds__(NWAVES * 64, 2) mk_fwd(Args args) {
;     ...
;         if (F.G == 256 && rep_ == 0) {
;             constexpr int NODD = CONV_SWA_ODD * 128 * NWAVES; const int lo = CONV_NITEMS - CONV_SWA;
;             const int rank = F.c >> 3, xcc = F.c & 7;
;             const bool att = F.loc ? (rank < 16) : ((F.c & 1) == 0);
;             const int half = F.loc ? (xcc * 16 + (rank & 15)) : (F.c >> 1), w = half * NWAVES + F.wave;
;             const int run = F.loc ? ((xcc >> 1) * 32 + (rank & 3) * 8 + (xcc & 1) * 4 + ((rank >> 2) & 3)) : half;
;             if (att) { swa_phase((char*)lds + RING_OFF, QO, KB, VB, XN, args.in[11], args.in[13], (LAS float*)(F.lds + RING_OFF + 100 * 1024), run, 128, F.wave);
;                        convert_items(F, args, lo + NODD, CONV_NITEMS, w, 128 * NWAVES); }
;             else convert_items(F, args, lo, lo + NODD, w, 128 * NWAVES); }
.LBB0_1325:
	s_and_b64 vcc, exec, s[0:1]
	s_cbranch_vccz .LBB0_1434
	s_ashr_i32 s4, s2, 3
	s_lshl_b32 s10, s2, 4
	s_and_b32 s0, s10, 0x70
	s_and_b32 s1, s4, 15
	v_readlane_b32 s6, v254, 24
	s_or_b32 s3, s0, s1
	s_ashr_i32 s11, s2, 1
	v_readlane_b32 s7, v254, 25
	s_and_b64 s[0:1], s[6:7], exec
	s_cselect_b32 s0, s11, s3
	s_lshl_b32 s3, s0, 3
	v_readlane_b32 s0, v254, 3
	s_add_i32 s3, s3, s0
	s_bitcmp0_b32 s2, 0
	s_cselect_b64 s[0:1], -1, 0
	s_cmp_lt_i32 s4, 16
	s_cselect_b64 s[4:5], -1, 0
	v_cndmask_b32_e64 v0, 0, 1, s[4:5]
	s_waitcnt lgkmcnt(0)
	v_cndmask_b32_e64 v1, 0, 1, s[0:1]
	v_cndmask_b32_e64 v0, v0, v1, s[6:7]
	v_and_b32_e32 v0, 1, v0
	v_cmp_eq_u32_e32 vcc, 0, v0
	s_mov_b64 s[0:1], -1
	s_cbranch_vccz .LBB0_1359
	s_cmpk_gt_i32 s3, 0x6bff
	v_mbcnt_lo_u32_b32 v4, -1, 0
	v_mbcnt_hi_u32_b32 v4, -1, v4
	s_cbranch_scc1 .LBB0_1358
	v_ashrrev_i32_e32 v30, 5, v4
	v_and_b32_e32 v28, 31, v4
	s_movk_i32 s0, 0x84
	v_lshlrev_b32_e32 v0, 2, v28
	v_mul_lo_u32 v2, v30, s0
	v_add3_u32 v31, s56, v0, v2
	v_lshlrev_b32_e32 v2, 4, v4
	v_ashrrev_i32_e32 v32, 2, v4
	v_and_b32_e32 v2, 48, v2
	v_and_b32_e32 v6, -4, v4
	v_ashrrev_i32_e32 v35, 3, v4
	v_lshlrev_b32_e32 v4, 3, v4
	v_mul_u32_u24_e32 v5, 0x84, v2
	v_and_b32_e32 v20, 56, v4
	v_readlane_b32 s40, v254, 5
	v_mov_b32_e32 v1, 0
	v_add3_u32 v33, s56, v5, v6
	v_mul_u32_u24_e32 v4, 0x84, v20
	v_lshlrev_b32_e32 v5, 2, v35
	v_readlane_b32 s41, v254, 6
	v_readlane_b32 s42, v254, 7
	v_readlane_b32 s43, v254, 8
	v_readlane_b32 s44, v254, 9
	v_readlane_b32 s45, v254, 10
	v_readlane_b32 s46, v254, 11
	v_readlane_b32 s47, v254, 12
	v_readlane_b32 s48, v254, 13
	v_readlane_b32 s49, v254, 14
	v_readlane_b32 s50, v254, 15
	v_readlane_b32 s51, v254, 16
	v_readlane_b32 s52, v254, 17
	v_readlane_b32 s53, v254, 18
	v_readlane_b32 s54, v254, 19
	v_readlane_b32 s55, v254, 20
	v_add3_u32 v36, s56, v4, v5
	v_lshl_add_u64 v[6:7], s[52:53], 0, v[0:1]
	v_lshl_add_u64 v[4:5], s[54:55], 0, v[0:1]
	v_lshl_add_u64 v[8:9], s[48:49], 0, v[0:1]
	v_lshl_add_u64 v[10:11], s[44:45], 0, v[0:1]
	v_lshl_add_u64 v[12:13], s[42:43], 0, v[0:1]
	v_readlane_b32 s40, v254, 36
	s_add_i32 s8, s3, 0x5a00
	v_readlane_b32 s54, v254, 50
	v_readlane_b32 s55, v254, 51
	v_mov_b32_e32 v3, v1
	s_lshl_b32 s0, s8, 1
	v_lshl_add_u64 v[14:15], s[54:55], 0, v[0:1]
	v_lshlrev_b32_e32 v0, 1, v20
	v_add_u32_e32 v34, 16, v32
	v_add_u32_e32 v37, 8, v35
	v_add_u32_e32 v38, 16, v35
	v_add_u32_e32 v39, 24, v35
	v_lshl_add_u64 v[16:17], s[26:27], 0, v[2:3]
	v_lshl_add_u64 v[18:19], s[60:61], 0, v[2:3]
	v_lshl_add_u64 v[20:21], s[62:63], 0, v[0:1]
	v_lshl_add_u64 v[22:23], s[64:65], 0, v[0:1]
	v_lshl_add_u64 v[24:25], s[84:85], 0, v[0:1]
	v_lshl_add_u64 v[26:27], s[86:87], 0, v[0:1]
	s_lshl_b32 s9, s8, 5
	s_add_i32 s12, s0, 0x1ca00
	s_mov_b32 s1, 0
	s_movk_i32 s13, 0xe00
	s_movk_i32 s14, 0x7000
	s_movk_i32 s15, 0x7fff
	s_mov_b32 s16, 0xffff0000
	s_movk_i32 s17, 0x1800
	s_movk_i32 s30, 0x3040
	v_lshlrev_b32_e32 v0, 2, v28
	v_add_u32_e32 v40, 0x400, v31
	v_add_u32_e32 v41, 0x800, v31
	v_add_u32_e32 v42, 0xc00, v31
	v_add_u32_e32 v43, 0x1000, v31
	v_add_u32_e32 v44, 0x1400, v31
	v_add_u32_e32 v45, 0x1800, v31
	v_add_u32_e32 v46, 0x1c00, v31
	v_add_u32_e32 v47, 0x400, v33
	v_readlane_b32 s41, v254, 37
	v_readlane_b32 s42, v254, 38
	v_readlane_b32 s43, v254, 39
	v_readlane_b32 s44, v254, 40
	v_readlane_b32 s45, v254, 41
	v_readlane_b32 s46, v254, 42
	v_readlane_b32 s47, v254, 43
	v_readlane_b32 s48, v254, 44
	v_readlane_b32 s49, v254, 45
	v_readlane_b32 s50, v254, 46
	v_readlane_b32 s51, v254, 47
	v_readlane_b32 s52, v254, 48
	v_readlane_b32 s53, v254, 49
	s_branch .LBB0_1330
.LBB0_1329:
	s_add_i32 s0, s8, 0x400
	s_add_i32 s9, s9, 0x8000
	s_addk_i32 s12, 0x800
	s_cmp_gt_i32 s8, 0xc1ff
	s_mov_b32 s8, s0
	s_cbranch_scc1 .LBB0_1358

; __device__ __forceinline__ int pg8_lane_id() { int l; asm volatile("v_mbcnt_lo_u32_b32 %0, -1, 0\n\tv_mbcnt_hi_u32_b32 %0, -1, %0" : "=v"(l)); return l; }
; #define LAS __attribute__((address_space(3)))
; __device__ __forceinline__ void convert_items(Frame& F, const Args& a, int lo, int hi, int w, int nw) {
;     const int lane = pg8::pg8_lane_id();
;     LAS float* scr = (LAS float*)(F.lds + RING_OFF + F.wave * 8448);
;     constexpr int I_FI = CONV_I_FI, I_FO = CONV_I_FO, I_SI = CONV_I_SI, I_SO = CONV_I_SO, I_GU = CONV_I_GU, I_DN = CONV_I_DN;
;     for (int it = lo + w; it < hi; it += nw) {
;         int r = it;
;         if (r < I_FI) { tr_item(a.in[7], 3 * D + 16, D, 96, r, (bf16*)(F.ws + WS_WFOXIN), false, scr, lane); continue; } r -= I_FI;
;         if (r < I_FO) { tr_item(a.in[9], D, D, 32, r, (bf16*)(F.ws + WS_WFOXOUT), false, scr, lane); continue; } r -= I_FO;
;         if (r < I_SI) { tr_item(a.in[10], D + 512, D, 48, r, (bf16*)(F.ws + WS_WSWAIN), false, scr, lane); continue; } r -= I_SI;
;         if (r < I_SO) { tr_item(a.in[12], D, D, 32, r, (bf16*)(F.ws + WS_WSWAOUT), false, scr, lane); continue; } r -= I_SO;
;         if (r < I_GU) { tr_item8(a.in[14], 2 * FF, D, 224, r, F.ws + WS_WGU, true, WSC_GU, scr, lane); continue; } r -= I_GU;
;         if (r < I_DN) { tr_item8(a.in[15], D, FF, 32, r, F.ws + WS_WDN, false, WSC_DN, scr, lane); continue; } r -= I_DN;
;         if (r < NE * I_GU) { const int e = r / I_GU, rr = r % I_GU; tr_item8(a.in[18] + (size_t)e * D * 2 * FF, 2 * FF, D, 224, rr, F.ws + WS_WMGU + (size_t)e * 2 * FF * D, true, WSC_GU, scr, lane); continue; } r -= NE * I_GU;
;         { const int e = r / I_DN, rr = r % I_DN; tr_item8(a.in[19] + (size_t)e * FF * D, D, FF, 32, rr, F.ws + WS_WMDN + (size_t)e * D * FF, false, WSC_DN, scr, lane); }
;     }
; }
; __global__ void __launch_bounds__(NWAVES * 64, 2) mk_fwd(Args args) {
;     ...
;             if (att) { swa_phase((char*)lds + RING_OFF, QO, KB, VB, XN, args.in[11], args.in[13], (LAS float*)(F.lds + RING_OFF + 100 * 1024), run, 128, F.wave);
;                        convert_items(F, args, lo + NODD, CONV_NITEMS, w, 128 * NWAVES); }
.LBB0_1403:
	s_cmpk_gt_i32 s3, 0x3ff
	s_barrier
	v_mbcnt_lo_u32_b32 v4, -1, 0
	v_mbcnt_hi_u32_b32 v4, -1, v4
	s_cbranch_scc1 .LBB0_1434
	v_ashrrev_i32_e32 v28, 5, v4
	v_and_b32_e32 v38, 31, v4
	s_movk_i32 s0, 0x84
	v_lshlrev_b32_e32 v0, 2, v38
	v_mul_lo_u32 v2, v28, s0
	v_add3_u32 v29, s56, v0, v2
	v_lshlrev_b32_e32 v2, 4, v4
	v_ashrrev_i32_e32 v30, 2, v4
	v_and_b32_e32 v2, 48, v2
	v_and_b32_e32 v6, -4, v4
	v_ashrrev_i32_e32 v33, 3, v4
	v_lshlrev_b32_e32 v4, 3, v4
	s_mov_b32 s90, s37
	s_mov_b32 s89, s36
	v_mul_u32_u24_e32 v5, 0x84, v2
	v_and_b32_e32 v20, 56, v4
	v_readlane_b32 s36, v254, 5
	v_mov_b32_e32 v1, 0
	v_add3_u32 v31, s56, v5, v6
	v_mul_u32_u24_e32 v4, 0x84, v20
	v_lshlrev_b32_e32 v5, 2, v33
	v_readlane_b32 s37, v254, 6
	v_readlane_b32 s38, v254, 7
	v_readlane_b32 s39, v254, 8
	v_readlane_b32 s40, v254, 9
	v_readlane_b32 s41, v254, 10
	v_readlane_b32 s42, v254, 11
	v_readlane_b32 s43, v254, 12
	v_readlane_b32 s44, v254, 13
	v_readlane_b32 s45, v254, 14
	v_readlane_b32 s46, v254, 15
	v_readlane_b32 s47, v254, 16
	v_readlane_b32 s48, v254, 17
	v_readlane_b32 s49, v254, 18
	v_readlane_b32 s50, v254, 19
	v_readlane_b32 s51, v254, 20
	v_add3_u32 v34, s56, v4, v5
	v_lshl_add_u64 v[6:7], s[48:49], 0, v[0:1]
	v_lshl_add_u64 v[4:5], s[50:51], 0, v[0:1]
	v_lshl_add_u64 v[8:9], s[44:45], 0, v[0:1]
	v_lshl_add_u64 v[10:11], s[40:41], 0, v[0:1]
	v_lshl_add_u64 v[12:13], s[38:39], 0, v[0:1]
	v_readlane_b32 s36, v254, 36
	s_add_i32 s3, s3, 0xc600
	v_readlane_b32 s50, v254, 50
	v_readlane_b32 s51, v254, 51
	v_mov_b32_e32 v3, v1
	v_readlane_b32 s37, v254, 37
	v_readlane_b32 s38, v254, 38
	v_readlane_b32 s39, v254, 39
	v_readlane_b32 s40, v254, 40
	v_readlane_b32 s41, v254, 41
	v_readlane_b32 s42, v254, 42
	v_readlane_b32 s43, v254, 43
	v_readlane_b32 s44, v254, 44
	v_readlane_b32 s45, v254, 45
	v_readlane_b32 s46, v254, 46
	v_readlane_b32 s47, v254, 47
	v_readlane_b32 s48, v254, 48
	v_readlane_b32 s49, v254, 49
	v_lshl_add_u64 v[14:15], s[50:51], 0, v[0:1]
	v_lshlrev_b32_e32 v0, 1, v20
	s_lshl_b32 s0, s3, 1
	v_readlane_b32 s68, v254, 28
	s_mov_b32 s88, s58
	v_add_u32_e32 v32, 16, v30
	v_add_u32_e32 v35, 8, v33
	v_add_u32_e32 v36, 16, v33
	v_add_u32_e32 v37, 24, v33
	v_lshl_add_u64 v[16:17], s[26:27], 0, v[2:3]
	v_lshl_add_u64 v[18:19], s[60:61], 0, v[2:3]
	v_lshl_add_u64 v[20:21], s[62:63], 0, v[0:1]
	v_lshl_add_u64 v[22:23], s[64:65], 0, v[0:1]
	v_lshl_add_u64 v[24:25], s[84:85], 0, v[0:1]
	v_lshl_add_u64 v[26:27], s[86:87], 0, v[0:1]
	s_lshl_b32 s8, s3, 5
	s_add_i32 s9, s0, 0x1ca00
	s_mov_b32 s1, 0
	s_movk_i32 s10, 0x2000
	s_movk_i32 s11, 0x4000
	s_movk_i32 s12, 0x6000
	s_mov_b32 s13, 0x8000
	s_mov_b32 s14, 0xa000
	s_mov_b32 s15, 0xc000
	s_mov_b32 s16, 0xe000
	s_mov_b32 s17, 0x10000
	s_mov_b32 s26, 0x12000
	s_mov_b32 s27, 0x14000
	s_mov_b32 s30, 0x16000
	s_mov_b32 s31, 0x18000
	s_mov_b32 s36, 0x1a000
	s_mov_b32 s37, 0x1c000
	s_mov_b32 s38, 0x1e000
	s_mov_b32 s39, 0x20000
	s_mov_b32 s40, 0x22000
	s_mov_b32 s41, 0x24000
	s_mov_b32 s42, 0x26000
	s_mov_b32 s43, 0x28000
	s_mov_b32 s44, 0x2a000
	s_mov_b32 s45, 0x2c000
	s_mov_b32 s46, 0x2e000
	s_mov_b32 s47, 0x30000
	s_mov_b32 s48, 0x32000
	s_mov_b32 s49, 0x34000
	s_mov_b32 s50, 0x36000
	s_mov_b32 s51, 0x38000
	s_mov_b32 s52, 0x3a000
	s_mov_b32 s53, 0x3c000
	s_mov_b32 s54, 0x3e000
	s_movk_i32 s55, 0xe00
	s_movk_i32 s56, 0x7000
	s_movk_i32 s57, 0x7fff
	s_mov_b32 s58, 0xffff0000
	s_movk_i32 s59, 0x1800
	s_movk_i32 s60, 0x3040
	v_lshlrev_b32_e32 v0, 2, v38
	v_add_u32_e32 v38, 0x400, v29
	v_add_u32_e32 v39, 0x800, v29
	v_add_u32_e32 v40, 0xc00, v29
	v_add_u32_e32 v41, 0x1000, v29
	v_add_u32_e32 v42, 0x1400, v29
	v_add_u32_e32 v43, 0x1800, v29
	v_add_u32_e32 v44, 0x1c00, v29
	v_add_u32_e32 v45, 0x400, v31
	v_readlane_b32 s72, v254, 32
	v_readlane_b32 s73, v254, 33
	v_readlane_b32 s74, v254, 34
	v_readlane_b32 s75, v254, 35
	v_readlane_b32 s69, v254, 29
	v_readlane_b32 s70, v254, 30
	v_readlane_b32 s71, v254, 31
	s_branch .LBB0_1406
